# expert GEMM2 epilogues: 14 of 16 pairs of 8-byte fp8 row stores merged into 16-byte stores after a v_permlane16_swap row exchange (on top of v75)
# speedup vs baseline: 1.0204x; 1.0064x over previous
.LBB0_1122:
	s_lshl_b32 s2, s87, 7
	v_add_u32_e32 v142, s80, v205
	v_add_u32_e32 v158, s81, v205
	s_add_u32 s64, s38, s2
	ds_read_b128 v[130:133], v142
	ds_read_b128 v[134:137], v142 offset:1024
	ds_read_b128 v[138:141], v142 offset:2048
	ds_read_b128 v[142:145], v142 offset:3072
	ds_read_b128 v[146:149], v158
	ds_read_b128 v[150:153], v158 offset:1024
	ds_read_b128 v[154:157], v158 offset:2048
	ds_read_b128 v[158:161], v158 offset:3072
	s_addc_u32 s65, s39, 0
	s_add_u32 s66, s64, 0x100
	s_addc_u32 s67, s65, 0
	s_and_b64 s[64:65], s[60:61], exec
	s_cselect_b32 s65, s35, s67
	s_cselect_b32 s64, s83, s66
	s_add_i32 s68, s2, 0x100
	s_and_b64 s[66:67], s[60:61], exec
	s_cselect_b32 s68, 0, s68
	s_add_u32 s2, s36, s2
	s_addc_u32 s67, s37, 0
	s_add_u32 s66, s2, 0x20080
	s_addc_u32 s67, s67, 0
	v_lshl_add_u64 v[210:211], s[66:67], 0, v[194:195]
	s_add_i32 m0, s50, 0xc000
	ds_read_b128 v[162:165], v209
	ds_read_b128 v[166:169], v209 offset:1024
	ds_read_b128 v[170:173], v209 offset:2048
	ds_read_b128 v[174:177], v209 offset:3072
	ds_read_b128 v[178:181], v209 offset:4096
	ds_read_b128 v[182:185], v209 offset:5120
	ds_read_b128 v[186:189], v209 offset:6144
	ds_read_b128 v[190:193], v209 offset:7168
	global_load_lds_dwordx4 v[210:211], off
	v_lshl_add_u64 v[210:211], s[66:67], 0, v[198:199]
	s_add_i32 m0, s50, 0xe000
	s_nop 0
	global_load_lds_dwordx4 v[210:211], off
	s_waitcnt vmcnt(8)
	s_waitcnt lgkmcnt(0)
	s_barrier
	s_waitcnt lgkmcnt(0)
	v_mfma_f32_16x16x32_bf16 v[86:89], v[130:133], v[162:165], v[86:89]
	v_mfma_f32_16x16x32_bf16 v[82:85], v[138:141], v[162:165], v[82:85]
	v_mfma_f32_16x16x32_bf16 v[78:81], v[130:133], v[170:173], v[78:81]
	v_mfma_f32_16x16x32_bf16 v[74:77], v[138:141], v[170:173], v[74:77]
	v_mfma_f32_16x16x32_bf16 v[70:73], v[130:133], v[178:181], v[70:73]
	v_mfma_f32_16x16x32_bf16 v[66:69], v[138:141], v[178:181], v[66:69]
	v_mfma_f32_16x16x32_bf16 v[62:65], v[130:133], v[186:189], v[62:65]
	v_mfma_f32_16x16x32_bf16 v[58:61], v[138:141], v[186:189], v[58:61]
	v_mfma_f32_16x16x32_bf16 v[86:89], v[134:137], v[166:169], v[86:89]
	v_mfma_f32_16x16x32_bf16 v[82:85], v[142:145], v[166:169], v[82:85]
	v_mfma_f32_16x16x32_bf16 v[78:81], v[134:137], v[174:177], v[78:81]
	v_mfma_f32_16x16x32_bf16 v[74:77], v[142:145], v[174:177], v[74:77]
	v_mfma_f32_16x16x32_bf16 v[70:73], v[134:137], v[182:185], v[70:73]
	v_mfma_f32_16x16x32_bf16 v[66:69], v[142:145], v[182:185], v[66:69]
	v_mfma_f32_16x16x32_bf16 v[62:65], v[134:137], v[190:193], v[62:65]
	v_mfma_f32_16x16x32_bf16 v[58:61], v[142:145], v[190:193], v[58:61]
	v_mfma_f32_16x16x32_bf16 v[54:57], v[146:149], v[162:165], v[54:57]
	v_mfma_f32_16x16x32_bf16 v[50:53], v[154:157], v[162:165], v[50:53]
	v_mfma_f32_16x16x32_bf16 v[46:49], v[146:149], v[170:173], v[46:49]
	v_mfma_f32_16x16x32_bf16 v[42:45], v[154:157], v[170:173], v[42:45]
	v_mfma_f32_16x16x32_bf16 v[34:37], v[146:149], v[178:181], v[34:37]
	v_mfma_f32_16x16x32_bf16 v[26:29], v[154:157], v[178:181], v[26:29]
	v_mfma_f32_16x16x32_bf16 v[18:21], v[146:149], v[186:189], v[18:21]
	v_mfma_f32_16x16x32_bf16 v[10:13], v[154:157], v[186:189], v[10:13]
	v_mfma_f32_16x16x32_bf16 v[54:57], v[150:153], v[166:169], v[54:57]
	v_mfma_f32_16x16x32_bf16 v[50:53], v[158:161], v[166:169], v[50:53]
	v_mfma_f32_16x16x32_bf16 v[46:49], v[150:153], v[174:177], v[46:49]
	v_mfma_f32_16x16x32_bf16 v[42:45], v[158:161], v[174:177], v[42:45]
	v_mfma_f32_16x16x32_bf16 v[34:37], v[150:153], v[182:185], v[34:37]
	v_mfma_f32_16x16x32_bf16 v[26:29], v[158:161], v[182:185], v[26:29]
	v_mfma_f32_16x16x32_bf16 v[18:21], v[150:153], v[190:193], v[18:21]
	v_mfma_f32_16x16x32_bf16 v[10:13], v[158:161], v[190:193], v[10:13]
	s_barrier
	s_add_i32 s2, s80, s49
	v_lshl_add_u64 v[210:211], s[64:65], 0, v[196:197]
	s_mov_b32 m0, s2
	ds_read_b128 v[162:165], v209 offset:16384
	ds_read_b128 v[166:169], v209 offset:17408
	ds_read_b128 v[170:173], v209 offset:18432
	ds_read_b128 v[174:177], v209 offset:19456
	ds_read_b128 v[178:181], v209 offset:20480
	ds_read_b128 v[182:185], v209 offset:21504
	ds_read_b128 v[186:189], v209 offset:22528
	ds_read_b128 v[190:193], v209 offset:23552
	global_load_lds_dwordx4 v[210:211], off
	s_add_i32 m0, s2, 0x2000
	s_add_u32 s66, s64, 0x20000
	v_lshl_add_u64 v[212:213], s[64:65], 0, v[200:201]
	s_addc_u32 s67, s65, 0
	s_add_i32 s2, s81, s49
	global_load_lds_dwordx4 v[212:213], off
	v_lshl_add_u64 v[214:215], s[66:67], 0, v[196:197]
	s_mov_b32 m0, s2
	s_nop 0
	global_load_lds_dwordx4 v[214:215], off
	s_add_i32 m0, s2, 0x2000
	s_add_u32 s62, s62, s68
	v_lshl_add_u64 v[214:215], s[66:67], 0, v[200:201]
	s_addc_u32 s63, s63, 0
	global_load_lds_dwordx4 v[214:215], off
	v_lshl_add_u64 v[214:215], s[62:63], 0, v[194:195]
	s_mov_b32 m0, s50
	v_lshl_add_u64 v[216:217], s[62:63], 0, v[198:199]
	global_load_lds_dwordx4 v[214:215], off
	s_mov_b32 m0, s51
	s_nop 0
	global_load_lds_dwordx4 v[216:217], off
	s_waitcnt vmcnt(8)
	s_waitcnt lgkmcnt(0)
	s_barrier
	s_waitcnt lgkmcnt(0)
	v_mfma_f32_16x16x32_bf16 v[126:129], v[130:133], v[162:165], v[126:129]
	v_mfma_f32_16x16x32_bf16 v[122:125], v[138:141], v[162:165], v[122:125]
	v_mfma_f32_16x16x32_bf16 v[110:113], v[130:133], v[170:173], v[110:113]
	v_mfma_f32_16x16x32_bf16 v[106:109], v[138:141], v[170:173], v[106:109]
	v_mfma_f32_16x16x32_bf16 v[94:97], v[130:133], v[178:181], v[94:97]
	v_mfma_f32_16x16x32_bf16 v[90:93], v[138:141], v[178:181], v[90:93]
	v_mfma_f32_16x16x32_bf16 v[22:25], v[130:133], v[186:189], v[22:25]
	v_mfma_f32_16x16x32_bf16 v[14:17], v[138:141], v[186:189], v[14:17]
	v_mfma_f32_16x16x32_bf16 v[126:129], v[134:137], v[166:169], v[126:129]
	v_mfma_f32_16x16x32_bf16 v[122:125], v[142:145], v[166:169], v[122:125]
	v_mfma_f32_16x16x32_bf16 v[110:113], v[134:137], v[174:177], v[110:113]
	v_mfma_f32_16x16x32_bf16 v[106:109], v[142:145], v[174:177], v[106:109]
	v_mfma_f32_16x16x32_bf16 v[94:97], v[134:137], v[182:185], v[94:97]
	v_mfma_f32_16x16x32_bf16 v[90:93], v[142:145], v[182:185], v[90:93]
	v_mfma_f32_16x16x32_bf16 v[22:25], v[134:137], v[190:193], v[22:25]
	v_mfma_f32_16x16x32_bf16 v[14:17], v[142:145], v[190:193], v[14:17]
	v_mfma_f32_16x16x32_bf16 v[118:121], v[146:149], v[162:165], v[118:121]
	v_mfma_f32_16x16x32_bf16 v[114:117], v[154:157], v[162:165], v[114:117]
	v_mfma_f32_16x16x32_bf16 v[102:105], v[146:149], v[170:173], v[102:105]
	v_mfma_f32_16x16x32_bf16 v[98:101], v[154:157], v[170:173], v[98:101]
	v_mfma_f32_16x16x32_bf16 v[38:41], v[146:149], v[178:181], v[38:41]
	v_mfma_f32_16x16x32_bf16 v[30:33], v[154:157], v[178:181], v[30:33]
	v_mfma_f32_16x16x32_bf16 v[6:9], v[146:149], v[186:189], v[6:9]
	v_mfma_f32_16x16x32_bf16 v[2:5], v[154:157], v[186:189], v[2:5]
	v_mfma_f32_16x16x32_bf16 v[118:121], v[150:153], v[166:169], v[118:121]
	v_mfma_f32_16x16x32_bf16 v[114:117], v[158:161], v[166:169], v[114:117]
	v_mfma_f32_16x16x32_bf16 v[102:105], v[150:153], v[174:177], v[102:105]
	v_mfma_f32_16x16x32_bf16 v[98:101], v[158:161], v[174:177], v[98:101]
	v_mfma_f32_16x16x32_bf16 v[38:41], v[150:153], v[182:185], v[38:41]
	v_mfma_f32_16x16x32_bf16 v[30:33], v[158:161], v[182:185], v[30:33]
	v_mfma_f32_16x16x32_bf16 v[6:9], v[150:153], v[190:193], v[6:9]
	v_mfma_f32_16x16x32_bf16 v[2:5], v[158:161], v[190:193], v[2:5]
	s_barrier
	s_add_i32 s2, 0, 0x18000
	s_add_i32 s66, 0, 0x1c000
	v_add_u32_e32 v130, s2, v205
	v_add_u32_e32 v142, s66, v205
	ds_read_b128 v[146:149], v130
	ds_read_b128 v[150:153], v130 offset:1024
	ds_read_b128 v[154:157], v130 offset:2048
	ds_read_b128 v[158:161], v130 offset:3072
	ds_read_b128 v[130:133], v142
	ds_read_b128 v[134:137], v142 offset:1024
	ds_read_b128 v[138:141], v142 offset:2048
	ds_read_b128 v[142:145], v142 offset:3072
	s_add_u32 s62, s62, 0x20000
	s_addc_u32 s63, s63, 0
	s_mov_b32 m0, s52
	v_lshl_add_u64 v[218:219], s[62:63], 0, v[194:195]
	ds_read_b128 v[162:165], v209 offset:32768
	ds_read_b128 v[166:169], v209 offset:33792
	ds_read_b128 v[170:173], v209 offset:34816
	ds_read_b128 v[174:177], v209 offset:35840
	ds_read_b128 v[178:181], v209 offset:36864
	ds_read_b128 v[182:185], v209 offset:37888
	ds_read_b128 v[186:189], v209 offset:38912
	ds_read_b128 v[190:193], v209 offset:39936
	global_load_lds_dwordx4 v[218:219], off
	v_lshl_add_u64 v[218:219], s[62:63], 0, v[198:199]
	s_mov_b32 m0, s53
	s_nop 0
	global_load_lds_dwordx4 v[218:219], off
	s_waitcnt vmcnt(8)
	s_waitcnt lgkmcnt(0)
	s_barrier
	s_waitcnt lgkmcnt(0)
	v_mfma_f32_16x16x32_bf16 v[86:89], v[146:149], v[162:165], v[86:89]
	v_mfma_f32_16x16x32_bf16 v[82:85], v[154:157], v[162:165], v[82:85]
	v_mfma_f32_16x16x32_bf16 v[78:81], v[146:149], v[170:173], v[78:81]
	v_mfma_f32_16x16x32_bf16 v[74:77], v[154:157], v[170:173], v[74:77]
	v_mfma_f32_16x16x32_bf16 v[70:73], v[146:149], v[178:181], v[70:73]
	v_mfma_f32_16x16x32_bf16 v[66:69], v[154:157], v[178:181], v[66:69]
	v_mfma_f32_16x16x32_bf16 v[62:65], v[146:149], v[186:189], v[62:65]
	v_mfma_f32_16x16x32_bf16 v[58:61], v[154:157], v[186:189], v[58:61]
	v_mfma_f32_16x16x32_bf16 v[86:89], v[150:153], v[166:169], v[86:89]
	v_mfma_f32_16x16x32_bf16 v[82:85], v[158:161], v[166:169], v[82:85]
	v_mfma_f32_16x16x32_bf16 v[78:81], v[150:153], v[174:177], v[78:81]
	v_mfma_f32_16x16x32_bf16 v[74:77], v[158:161], v[174:177], v[74:77]
	v_mfma_f32_16x16x32_bf16 v[70:73], v[150:153], v[182:185], v[70:73]
	v_mfma_f32_16x16x32_bf16 v[66:69], v[158:161], v[182:185], v[66:69]
	v_mfma_f32_16x16x32_bf16 v[62:65], v[150:153], v[190:193], v[62:65]
	v_mfma_f32_16x16x32_bf16 v[58:61], v[158:161], v[190:193], v[58:61]
	v_mfma_f32_16x16x32_bf16 v[54:57], v[130:133], v[162:165], v[54:57]
	v_mfma_f32_16x16x32_bf16 v[50:53], v[138:141], v[162:165], v[50:53]
	v_mfma_f32_16x16x32_bf16 v[46:49], v[130:133], v[170:173], v[46:49]
	v_mfma_f32_16x16x32_bf16 v[42:45], v[138:141], v[170:173], v[42:45]
	v_mfma_f32_16x16x32_bf16 v[34:37], v[130:133], v[178:181], v[34:37]
	v_mfma_f32_16x16x32_bf16 v[26:29], v[138:141], v[178:181], v[26:29]
	v_mfma_f32_16x16x32_bf16 v[18:21], v[130:133], v[186:189], v[18:21]
	v_mfma_f32_16x16x32_bf16 v[10:13], v[138:141], v[186:189], v[10:13]
	v_mfma_f32_16x16x32_bf16 v[54:57], v[134:137], v[166:169], v[54:57]
	v_mfma_f32_16x16x32_bf16 v[50:53], v[142:145], v[166:169], v[50:53]
	v_mfma_f32_16x16x32_bf16 v[46:49], v[134:137], v[174:177], v[46:49]
	v_mfma_f32_16x16x32_bf16 v[42:45], v[142:145], v[174:177], v[42:45]
	v_mfma_f32_16x16x32_bf16 v[34:37], v[134:137], v[182:185], v[34:37]
	v_mfma_f32_16x16x32_bf16 v[26:29], v[142:145], v[182:185], v[26:29]
	v_mfma_f32_16x16x32_bf16 v[18:21], v[134:137], v[190:193], v[18:21]
	v_mfma_f32_16x16x32_bf16 v[10:13], v[142:145], v[190:193], v[10:13]
	s_barrier
	s_add_i32 s2, s2, s49
	v_lshl_add_u64 v[210:211], v[210:211], 0, s[12:13]
	s_mov_b32 m0, s2
	ds_read_b128 v[186:189], v209 offset:49152
	ds_read_b128 v[190:193], v209 offset:50176
	ds_read_b128 v[178:181], v209 offset:51200
	ds_read_b128 v[182:185], v209 offset:52224
	ds_read_b128 v[170:173], v209 offset:53248
	ds_read_b128 v[174:177], v209 offset:54272
	ds_read_b128 v[162:165], v209 offset:55296
	ds_read_b128 v[166:169], v209 offset:56320
	global_load_lds_dwordx4 v[210:211], off
	s_add_i32 m0, s2, 0x2000
	s_add_u32 s62, s64, 0x20080
	v_lshl_add_u64 v[210:211], v[212:213], 0, s[12:13]
	s_addc_u32 s63, s65, 0
	s_add_i32 s2, s66, s49
	global_load_lds_dwordx4 v[210:211], off
	v_lshl_add_u64 v[210:211], s[62:63], 0, v[196:197]
	s_mov_b32 m0, s2
	s_andn2_b64 vcc, exec, s[60:61]
	global_load_lds_dwordx4 v[210:211], off
	v_lshl_add_u64 v[210:211], s[62:63], 0, v[200:201]
	s_add_i32 m0, s2, 0x2000
	s_nop 0
	global_load_lds_dwordx4 v[210:211], off
	v_lshl_add_u64 v[210:211], v[214:215], 0, s[12:13]
	s_mov_b32 m0, s73
	s_nop 0
	global_load_lds_dwordx4 v[210:211], off
	v_lshl_add_u64 v[210:211], v[216:217], 0, s[12:13]
	s_mov_b32 m0, s74
	s_nop 0
	global_load_lds_dwordx4 v[210:211], off
	s_waitcnt vmcnt(8)
	s_waitcnt lgkmcnt(0)
	s_barrier
	s_cbranch_vccnz .LBB0_1104
	v_pk_mul_f32 v[214:215], v[86:87], s[20:21] op_sel_hi:[1,0]
	v_pk_mul_f32 v[216:217], v[82:83], s[20:21] op_sel_hi:[1,0]
	v_mov_b32_e32 v218, 0
	v_mov_b32_e32 v219, 0
	v_cvt_pk_fp8_f32 v218, v214, v215
	v_cvt_pk_fp8_f32 v219, v216, v217
	v_pk_mul_f32 v[214:215], v[88:89], s[20:21] op_sel_hi:[1,0]
	v_pk_mul_f32 v[216:217], v[84:85], s[20:21] op_sel_hi:[1,0]
	v_cvt_pk_fp8_f32 v218, v214, v215 op_sel:[0,0,1]
	v_cvt_pk_fp8_f32 v219, v216, v217 op_sel:[0,0,1]
	v_pk_mul_f32 v[214:215], v[54:55], s[20:21] op_sel_hi:[1,0]
	v_pk_mul_f32 v[216:217], v[50:51], s[20:21] op_sel_hi:[1,0]
	v_mov_b32_e32 v220, 0
	v_mov_b32_e32 v221, 0
	v_mov_b32_e32 v210, v1
	v_mov_b32_e32 v211, v204
	v_cvt_pk_fp8_f32 v220, v214, v215
	v_cvt_pk_fp8_f32 v221, v216, v217
	v_pk_mul_f32 v[214:215], v[56:57], s[20:21] op_sel_hi:[1,0]
	v_add_u32_e32 v210, s85, v210
	v_lshl_add_u32 v212, v211, 3, s86
	v_ashrrev_i32_e32 v211, 31, v210
	v_pk_mul_f32 v[216:217], v[52:53], s[20:21] op_sel_hi:[1,0]
	v_lshlrev_b64 v[210:211], 11, v[210:211]
	v_cvt_pk_fp8_f32 v220, v214, v215 op_sel:[0,0,1]
	v_cvt_pk_fp8_f32 v221, v216, v217 op_sel:[0,0,1]
	v_ashrrev_i32_e32 v213, 31, v212
	v_lshl_add_u64 v[210:211], s[10:11], 0, v[210:211]
	v_lshl_add_u64 v[210:211], v[210:211], 0, v[212:213]
	s_nop 1
	v_permlane16_swap_b32 v218, v220
	v_permlane16_swap_b32 v219, v221
	v_and_b32_e32 v216, 1, v204
	v_mul_u32_u24_e32 v216, 0x78, v216
	v_mov_b32_e32 v217, 0
	v_lshl_add_u64 v[216:217], v[210:211], 0, v[216:217]
	global_store_dwordx4 v[216:217], v[218:221], off
	v_pk_mul_f32 v[214:215], v[78:79], s[20:21] op_sel_hi:[1,0]
	v_pk_mul_f32 v[216:217], v[74:75], s[20:21] op_sel_hi:[1,0]
	v_mov_b32_e32 v218, 0
	v_mov_b32_e32 v219, 0
	v_cvt_pk_fp8_f32 v218, v214, v215
	v_cvt_pk_fp8_f32 v219, v216, v217
	v_pk_mul_f32 v[214:215], v[80:81], s[20:21] op_sel_hi:[1,0]
	v_pk_mul_f32 v[216:217], v[76:77], s[20:21] op_sel_hi:[1,0]
	v_cvt_pk_fp8_f32 v218, v214, v215 op_sel:[0,0,1]
	v_cvt_pk_fp8_f32 v219, v216, v217 op_sel:[0,0,1]
	v_pk_mul_f32 v[214:215], v[46:47], s[20:21] op_sel_hi:[1,0]
	v_pk_mul_f32 v[216:217], v[42:43], s[20:21] op_sel_hi:[1,0]
	v_mov_b32_e32 v220, 0
	v_mov_b32_e32 v221, 0
	v_cvt_pk_fp8_f32 v220, v214, v215
	v_cvt_pk_fp8_f32 v221, v216, v217
	v_pk_mul_f32 v[214:215], v[48:49], s[20:21] op_sel_hi:[1,0]
	v_pk_mul_f32 v[216:217], v[44:45], s[20:21] op_sel_hi:[1,0]
	v_cvt_pk_fp8_f32 v220, v214, v215 op_sel:[0,0,1]
	v_cvt_pk_fp8_f32 v221, v216, v217 op_sel:[0,0,1]
	s_mov_b32 s2, 0x8000
	v_add_co_u32_e32 v214, vcc, s2, v210
	s_mov_b64 s[60:61], 0x8000
	s_nop 0
	v_addc_co_u32_e32 v215, vcc, 0, v211, vcc
	v_lshl_add_u64 v[212:213], v[210:211], 0, s[60:61]
	s_nop 1
	v_permlane16_swap_b32 v218, v220
	v_permlane16_swap_b32 v219, v221
	v_and_b32_e32 v216, 1, v204
	v_mul_u32_u24_e32 v216, 0x78, v216
	v_mov_b32_e32 v217, 0
	v_lshl_add_u64 v[216:217], v[214:215], 0, v[216:217]
	global_store_dwordx4 v[216:217], v[218:221], off
	v_pk_mul_f32 v[214:215], v[70:71], s[20:21] op_sel_hi:[1,0]
	v_pk_mul_f32 v[216:217], v[66:67], s[20:21] op_sel_hi:[1,0]
	v_mov_b32_e32 v218, 0
	v_mov_b32_e32 v219, 0
	v_cvt_pk_fp8_f32 v218, v214, v215
	v_cvt_pk_fp8_f32 v219, v216, v217
	v_pk_mul_f32 v[214:215], v[72:73], s[20:21] op_sel_hi:[1,0]
	v_pk_mul_f32 v[216:217], v[68:69], s[20:21] op_sel_hi:[1,0]
	v_cvt_pk_fp8_f32 v218, v214, v215 op_sel:[0,0,1]
	v_cvt_pk_fp8_f32 v219, v216, v217 op_sel:[0,0,1]
	v_pk_mul_f32 v[214:215], v[34:35], s[20:21] op_sel_hi:[1,0]
	v_pk_mul_f32 v[216:217], v[26:27], s[20:21] op_sel_hi:[1,0]
	v_mov_b32_e32 v220, 0
	v_mov_b32_e32 v221, 0
	v_cvt_pk_fp8_f32 v220, v214, v215
	v_cvt_pk_fp8_f32 v221, v216, v217
	v_pk_mul_f32 v[214:215], v[36:37], s[20:21] op_sel_hi:[1,0]
	v_pk_mul_f32 v[216:217], v[28:29], s[20:21] op_sel_hi:[1,0]
	v_cvt_pk_fp8_f32 v220, v214, v215 op_sel:[0,0,1]
	v_cvt_pk_fp8_f32 v221, v216, v217 op_sel:[0,0,1]
	s_mov_b32 s2, 0x10000
	v_add_co_u32_e32 v214, vcc, s2, v210
	v_lshl_add_u64 v[212:213], v[210:211], 0, s[24:25]
	s_nop 0
	v_addc_co_u32_e32 v215, vcc, 0, v211, vcc
	s_nop 1
	v_permlane16_swap_b32 v218, v220
	v_permlane16_swap_b32 v219, v221
	v_and_b32_e32 v216, 1, v204
	v_mul_u32_u24_e32 v216, 0x78, v216
	v_mov_b32_e32 v217, 0
	v_lshl_add_u64 v[216:217], v[214:215], 0, v[216:217]
	global_store_dwordx4 v[216:217], v[218:221], off
	v_pk_mul_f32 v[214:215], v[62:63], s[20:21] op_sel_hi:[1,0]
	v_pk_mul_f32 v[216:217], v[58:59], s[20:21] op_sel_hi:[1,0]
	v_mov_b32_e32 v218, 0
	v_mov_b32_e32 v219, 0
	v_cvt_pk_fp8_f32 v218, v214, v215
	v_cvt_pk_fp8_f32 v219, v216, v217
	v_pk_mul_f32 v[214:215], v[64:65], s[20:21] op_sel_hi:[1,0]
	v_pk_mul_f32 v[216:217], v[60:61], s[20:21] op_sel_hi:[1,0]
	v_cvt_pk_fp8_f32 v218, v214, v215 op_sel:[0,0,1]
	v_cvt_pk_fp8_f32 v219, v216, v217 op_sel:[0,0,1]
	v_pk_mul_f32 v[214:215], v[18:19], s[20:21] op_sel_hi:[1,0]
	v_pk_mul_f32 v[216:217], v[10:11], s[20:21] op_sel_hi:[1,0]
	v_mov_b32_e32 v220, 0
	v_mov_b32_e32 v221, 0
	v_cvt_pk_fp8_f32 v220, v214, v215
	v_cvt_pk_fp8_f32 v221, v216, v217
	v_pk_mul_f32 v[214:215], v[20:21], s[20:21] op_sel_hi:[1,0]
	v_pk_mul_f32 v[216:217], v[12:13], s[20:21] op_sel_hi:[1,0]
	v_cvt_pk_fp8_f32 v220, v214, v215 op_sel:[0,0,1]
	v_cvt_pk_fp8_f32 v221, v216, v217 op_sel:[0,0,1]
	s_mov_b32 s2, 0x18000
	v_lshl_add_u64 v[212:213], v[210:211], 0, s[28:29]
	v_add_co_u32_e32 v210, vcc, s2, v210
	s_nop 1
	v_addc_co_u32_e32 v211, vcc, 0, v211, vcc
	s_nop 1
	v_permlane16_swap_b32 v218, v220
	v_permlane16_swap_b32 v219, v221
	v_and_b32_e32 v216, 1, v204
	v_mul_u32_u24_e32 v216, 0x78, v216
	v_mov_b32_e32 v217, 0
	v_lshl_add_u64 v[216:217], v[210:211], 0, v[216:217]
	global_store_dwordx4 v[216:217], v[218:221], off
	s_branch .LBB0_1104

.LBB0_1126:
	v_pk_mul_f32 v[20:21], v[126:127], s[20:21] op_sel_hi:[1,0]
	v_pk_mul_f32 v[26:27], v[122:123], s[20:21] op_sel_hi:[1,0]
	v_mov_b32_e32 v42, 0
	v_mov_b32_e32 v43, 0
	v_cvt_pk_fp8_f32 v42, v20, v21
	v_cvt_pk_fp8_f32 v43, v26, v27
	v_pk_mul_f32 v[20:21], v[128:129], s[20:21] op_sel_hi:[1,0]
	v_pk_mul_f32 v[26:27], v[124:125], s[20:21] op_sel_hi:[1,0]
	v_cvt_pk_fp8_f32 v42, v20, v21 op_sel:[0,0,1]
	v_cvt_pk_fp8_f32 v43, v26, v27 op_sel:[0,0,1]
	v_pk_mul_f32 v[20:21], v[118:119], s[20:21] op_sel_hi:[1,0]
	v_pk_mul_f32 v[26:27], v[114:115], s[20:21] op_sel_hi:[1,0]
	v_mov_b32_e32 v44, 0
	v_mov_b32_e32 v45, 0
	v_cvt_pk_fp8_f32 v44, v20, v21
	v_cvt_pk_fp8_f32 v45, v26, v27
	v_add_u32_e32 v12, s31, v206
	v_ashrrev_i32_e32 v13, 31, v12
	v_pk_mul_f32 v[20:21], v[120:121], s[20:21] op_sel_hi:[1,0]
	v_pk_mul_f32 v[26:27], v[116:117], s[20:21] op_sel_hi:[1,0]
	v_or_b32_e32 v10, s84, v207
	v_lshlrev_b64 v[18:19], 11, v[12:13]
	v_cvt_pk_fp8_f32 v44, v20, v21 op_sel:[0,0,1]
	v_cvt_pk_fp8_f32 v45, v26, v27 op_sel:[0,0,1]
	v_ashrrev_i32_e32 v11, 31, v10
	v_lshl_add_u64 v[18:19], s[10:11], 0, v[18:19]
	v_lshl_add_u64 v[18:19], v[18:19], 0, v[10:11]
	s_nop 1
	v_permlane16_swap_b32 v42, v44
	v_permlane16_swap_b32 v43, v45
	v_and_b32_e32 v26, 1, v204
	v_mul_u32_u24_e32 v26, 0x78, v26
	v_mov_b32_e32 v27, 0
	v_lshl_add_u64 v[26:27], v[18:19], 0, v[26:27]
	global_store_dwordx4 v[26:27], v[42:45], off
	v_pk_mul_f32 v[20:21], v[110:111], s[20:21] op_sel_hi:[1,0]
	v_pk_mul_f32 v[26:27], v[106:107], s[20:21] op_sel_hi:[1,0]
	v_mov_b32_e32 v46, 0
	v_mov_b32_e32 v47, 0
	v_cvt_pk_fp8_f32 v46, v20, v21
	v_cvt_pk_fp8_f32 v47, v26, v27
	v_pk_mul_f32 v[20:21], v[112:113], s[20:21] op_sel_hi:[1,0]
	v_pk_mul_f32 v[26:27], v[108:109], s[20:21] op_sel_hi:[1,0]
	v_cvt_pk_fp8_f32 v46, v20, v21 op_sel:[0,0,1]
	v_cvt_pk_fp8_f32 v47, v26, v27 op_sel:[0,0,1]
	v_pk_mul_f32 v[20:21], v[102:103], s[20:21] op_sel_hi:[1,0]
	v_pk_mul_f32 v[26:27], v[98:99], s[20:21] op_sel_hi:[1,0]
	v_mov_b32_e32 v48, 0
	v_mov_b32_e32 v49, 0
	v_cvt_pk_fp8_f32 v48, v20, v21
	v_cvt_pk_fp8_f32 v49, v26, v27
	v_or_b32_e32 v18, 16, v12
	v_ashrrev_i32_e32 v19, 31, v18
	v_pk_mul_f32 v[20:21], v[104:105], s[20:21] op_sel_hi:[1,0]
	v_pk_mul_f32 v[26:27], v[100:101], s[20:21] op_sel_hi:[1,0]
	v_lshlrev_b64 v[18:19], 11, v[18:19]
	v_cvt_pk_fp8_f32 v48, v20, v21 op_sel:[0,0,1]
	v_cvt_pk_fp8_f32 v49, v26, v27 op_sel:[0,0,1]
	v_lshl_add_u64 v[18:19], s[10:11], 0, v[18:19]
	v_lshl_add_u64 v[18:19], v[18:19], 0, v[10:11]
	s_nop 1
	v_permlane16_swap_b32 v46, v48
	v_permlane16_swap_b32 v47, v49
	v_and_b32_e32 v26, 1, v204
	v_mul_u32_u24_e32 v26, 0x78, v26
	v_mov_b32_e32 v27, 0
	v_lshl_add_u64 v[26:27], v[18:19], 0, v[26:27]
	global_store_dwordx4 v[26:27], v[46:49], off
	v_pk_mul_f32 v[20:21], v[94:95], s[20:21] op_sel_hi:[1,0]
	v_pk_mul_f32 v[26:27], v[90:91], s[20:21] op_sel_hi:[1,0]
	v_mov_b32_e32 v28, 0
	v_mov_b32_e32 v29, 0
	v_cvt_pk_fp8_f32 v28, v20, v21
	v_cvt_pk_fp8_f32 v29, v26, v27
	v_pk_mul_f32 v[20:21], v[96:97], s[20:21] op_sel_hi:[1,0]
	v_pk_mul_f32 v[26:27], v[92:93], s[20:21] op_sel_hi:[1,0]
	v_cvt_pk_fp8_f32 v28, v20, v21 op_sel:[0,0,1]
	v_cvt_pk_fp8_f32 v29, v26, v27 op_sel:[0,0,1]
	v_pk_mul_f32 v[20:21], v[38:39], s[20:21] op_sel_hi:[1,0]
	v_pk_mul_f32 v[26:27], v[30:31], s[20:21] op_sel_hi:[1,0]
	v_mov_b32_e32 v30, 0
	v_mov_b32_e32 v31, 0
	v_cvt_pk_fp8_f32 v30, v20, v21
	v_cvt_pk_fp8_f32 v31, v26, v27
	v_or_b32_e32 v18, 32, v12
	v_ashrrev_i32_e32 v19, 31, v18
	v_pk_mul_f32 v[20:21], v[40:41], s[20:21] op_sel_hi:[1,0]
	v_pk_mul_f32 v[26:27], v[32:33], s[20:21] op_sel_hi:[1,0]
	v_lshlrev_b64 v[18:19], 11, v[18:19]
	v_cvt_pk_fp8_f32 v30, v20, v21 op_sel:[0,0,1]
	v_cvt_pk_fp8_f32 v31, v26, v27 op_sel:[0,0,1]
	v_lshl_add_u64 v[18:19], s[10:11], 0, v[18:19]
	v_lshl_add_u64 v[18:19], v[18:19], 0, v[10:11]
	s_nop 1
	v_permlane16_swap_b32 v28, v30
	v_permlane16_swap_b32 v29, v31
	v_and_b32_e32 v26, 1, v204
	v_mul_u32_u24_e32 v26, 0x78, v26
	v_mov_b32_e32 v27, 0
	v_lshl_add_u64 v[26:27], v[18:19], 0, v[26:27]
	global_store_dwordx4 v[26:27], v[28:31], off
	v_pk_mul_f32 v[18:19], v[22:23], s[20:21] op_sel_hi:[1,0]
	v_mov_b32_e32 v20, 0
	v_cvt_pk_fp8_f32 v20, v18, v19
	v_pk_mul_f32 v[14:15], v[14:15], s[20:21] op_sel_hi:[1,0]
	v_mov_b32_e32 v21, 0
	v_cvt_pk_fp8_f32 v21, v14, v15
	v_pk_mul_f32 v[14:15], v[24:25], s[20:21] op_sel_hi:[1,0]
	v_pk_mul_f32 v[6:7], v[6:7], s[20:21] op_sel_hi:[1,0]
	v_cvt_pk_fp8_f32 v20, v14, v15 op_sel:[0,0,1]
	v_pk_mul_f32 v[2:3], v[2:3], s[20:21] op_sel_hi:[1,0]
	v_mov_b32_e32 v14, 0
	v_mov_b32_e32 v15, 0
	v_cvt_pk_fp8_f32 v14, v6, v7
	v_cvt_pk_fp8_f32 v15, v2, v3
	v_or_b32_e32 v12, 48, v12
	v_pk_mul_f32 v[16:17], v[16:17], s[20:21] op_sel_hi:[1,0]
	v_ashrrev_i32_e32 v13, 31, v12
	v_cvt_pk_fp8_f32 v21, v16, v17 op_sel:[0,0,1]
	v_pk_mul_f32 v[2:3], v[8:9], s[20:21] op_sel_hi:[1,0]
	v_pk_mul_f32 v[4:5], v[4:5], s[20:21] op_sel_hi:[1,0]
	v_lshlrev_b64 v[12:13], 11, v[12:13]
	v_cvt_pk_fp8_f32 v14, v2, v3 op_sel:[0,0,1]
	v_cvt_pk_fp8_f32 v15, v4, v5 op_sel:[0,0,1]
	v_lshl_add_u64 v[2:3], s[10:11], 0, v[12:13]
	v_lshl_add_u64 v[2:3], v[2:3], 0, v[10:11]
	s_andn2_b64 vcc, exec, s[40:41]
	s_mov_b64 s[36:37], -1
	global_store_dwordx2 v[2:3], v[20:21], off
	global_store_dwordx2 v[2:3], v[14:15], off offset:128
	s_cbranch_vccnz .LBB0_1093
	s_andn2_b64 vcc, exec, s[8:9]
	s_cbranch_vccnz .LBB0_1092
	s_barrier
	s_branch .LBB0_1092

.LBB0_1954:
	s_lshl_b32 s2, s89, 7
	v_add_u32_e32 v142, s82, v205
	v_add_u32_e32 v158, s83, v205
	s_add_u32 s66, s40, s2
	ds_read_b128 v[130:133], v142
	ds_read_b128 v[134:137], v142 offset:1024
	ds_read_b128 v[138:141], v142 offset:2048
	ds_read_b128 v[142:145], v142 offset:3072
	ds_read_b128 v[146:149], v158
	ds_read_b128 v[150:153], v158 offset:1024
	ds_read_b128 v[154:157], v158 offset:2048
	ds_read_b128 v[158:161], v158 offset:3072
	s_addc_u32 s67, s41, 0
	s_add_u32 s68, s66, 0x100
	s_addc_u32 s69, s67, 0
	s_and_b64 s[66:67], s[62:63], exec
	s_cselect_b32 s67, s37, s69
	s_cselect_b32 s66, s85, s68
	s_add_i32 s70, s2, 0x100
	s_and_b64 s[68:69], s[62:63], exec
	s_cselect_b32 s70, 0, s70
	s_add_u32 s2, s38, s2
	s_addc_u32 s69, s39, 0
	s_add_u32 s68, s2, 0x20080
	s_addc_u32 s69, s69, 0
	v_lshl_add_u64 v[210:211], s[68:69], 0, v[194:195]
	s_add_i32 m0, s50, 0xc000
	ds_read_b128 v[162:165], v209
	ds_read_b128 v[166:169], v209 offset:1024
	ds_read_b128 v[170:173], v209 offset:2048
	ds_read_b128 v[174:177], v209 offset:3072
	ds_read_b128 v[178:181], v209 offset:4096
	ds_read_b128 v[182:185], v209 offset:5120
	ds_read_b128 v[186:189], v209 offset:6144
	ds_read_b128 v[190:193], v209 offset:7168
	global_load_lds_dwordx4 v[210:211], off
	v_lshl_add_u64 v[210:211], s[68:69], 0, v[198:199]
	s_add_i32 m0, s50, 0xe000
	s_nop 0
	global_load_lds_dwordx4 v[210:211], off
	s_waitcnt vmcnt(8)
	s_waitcnt lgkmcnt(0)
	s_barrier
	s_waitcnt lgkmcnt(0)
	v_mfma_f32_16x16x32_bf16 v[86:89], v[130:133], v[162:165], v[86:89]
	v_mfma_f32_16x16x32_bf16 v[82:85], v[138:141], v[162:165], v[82:85]
	v_mfma_f32_16x16x32_bf16 v[78:81], v[130:133], v[170:173], v[78:81]
	v_mfma_f32_16x16x32_bf16 v[74:77], v[138:141], v[170:173], v[74:77]
	v_mfma_f32_16x16x32_bf16 v[70:73], v[130:133], v[178:181], v[70:73]
	v_mfma_f32_16x16x32_bf16 v[66:69], v[138:141], v[178:181], v[66:69]
	v_mfma_f32_16x16x32_bf16 v[62:65], v[130:133], v[186:189], v[62:65]
	v_mfma_f32_16x16x32_bf16 v[58:61], v[138:141], v[186:189], v[58:61]
	v_mfma_f32_16x16x32_bf16 v[86:89], v[134:137], v[166:169], v[86:89]
	v_mfma_f32_16x16x32_bf16 v[82:85], v[142:145], v[166:169], v[82:85]
	v_mfma_f32_16x16x32_bf16 v[78:81], v[134:137], v[174:177], v[78:81]
	v_mfma_f32_16x16x32_bf16 v[74:77], v[142:145], v[174:177], v[74:77]
	v_mfma_f32_16x16x32_bf16 v[70:73], v[134:137], v[182:185], v[70:73]
	v_mfma_f32_16x16x32_bf16 v[66:69], v[142:145], v[182:185], v[66:69]
	v_mfma_f32_16x16x32_bf16 v[62:65], v[134:137], v[190:193], v[62:65]
	v_mfma_f32_16x16x32_bf16 v[58:61], v[142:145], v[190:193], v[58:61]
	v_mfma_f32_16x16x32_bf16 v[54:57], v[146:149], v[162:165], v[54:57]
	v_mfma_f32_16x16x32_bf16 v[50:53], v[154:157], v[162:165], v[50:53]
	v_mfma_f32_16x16x32_bf16 v[46:49], v[146:149], v[170:173], v[46:49]
	v_mfma_f32_16x16x32_bf16 v[42:45], v[154:157], v[170:173], v[42:45]
	v_mfma_f32_16x16x32_bf16 v[34:37], v[146:149], v[178:181], v[34:37]
	v_mfma_f32_16x16x32_bf16 v[30:33], v[154:157], v[178:181], v[30:33]
	v_mfma_f32_16x16x32_bf16 v[18:21], v[146:149], v[186:189], v[18:21]
	v_mfma_f32_16x16x32_bf16 v[14:17], v[154:157], v[186:189], v[14:17]
	v_mfma_f32_16x16x32_bf16 v[54:57], v[150:153], v[166:169], v[54:57]
	v_mfma_f32_16x16x32_bf16 v[50:53], v[158:161], v[166:169], v[50:53]
	v_mfma_f32_16x16x32_bf16 v[46:49], v[150:153], v[174:177], v[46:49]
	v_mfma_f32_16x16x32_bf16 v[42:45], v[158:161], v[174:177], v[42:45]
	v_mfma_f32_16x16x32_bf16 v[34:37], v[150:153], v[182:185], v[34:37]
	v_mfma_f32_16x16x32_bf16 v[30:33], v[158:161], v[182:185], v[30:33]
	v_mfma_f32_16x16x32_bf16 v[18:21], v[150:153], v[190:193], v[18:21]
	v_mfma_f32_16x16x32_bf16 v[14:17], v[158:161], v[190:193], v[14:17]
	s_barrier
	s_add_i32 s2, s82, s49
	v_lshl_add_u64 v[210:211], s[66:67], 0, v[196:197]
	s_mov_b32 m0, s2
	ds_read_b128 v[162:165], v209 offset:16384
	ds_read_b128 v[166:169], v209 offset:17408
	ds_read_b128 v[170:173], v209 offset:18432
	ds_read_b128 v[174:177], v209 offset:19456
	ds_read_b128 v[178:181], v209 offset:20480
	ds_read_b128 v[182:185], v209 offset:21504
	ds_read_b128 v[186:189], v209 offset:22528
	ds_read_b128 v[190:193], v209 offset:23552
	global_load_lds_dwordx4 v[210:211], off
	s_add_i32 m0, s2, 0x2000
	s_add_u32 s68, s66, 0x20000
	v_lshl_add_u64 v[212:213], s[66:67], 0, v[200:201]
	s_addc_u32 s69, s67, 0
	s_add_i32 s2, s83, s49
	global_load_lds_dwordx4 v[212:213], off
	v_lshl_add_u64 v[214:215], s[68:69], 0, v[196:197]
	s_mov_b32 m0, s2
	s_nop 0
	global_load_lds_dwordx4 v[214:215], off
	s_add_i32 m0, s2, 0x2000
	s_add_u32 s64, s64, s70
	v_lshl_add_u64 v[214:215], s[68:69], 0, v[200:201]
	s_addc_u32 s65, s65, 0
	global_load_lds_dwordx4 v[214:215], off
	v_lshl_add_u64 v[214:215], s[64:65], 0, v[194:195]
	s_mov_b32 m0, s50
	v_lshl_add_u64 v[216:217], s[64:65], 0, v[198:199]
	global_load_lds_dwordx4 v[214:215], off
	s_mov_b32 m0, s51
	s_nop 0
	global_load_lds_dwordx4 v[216:217], off
	s_waitcnt vmcnt(8)
	s_waitcnt lgkmcnt(0)
	s_barrier
	s_waitcnt lgkmcnt(0)
	v_mfma_f32_16x16x32_bf16 v[126:129], v[130:133], v[162:165], v[126:129]
	v_mfma_f32_16x16x32_bf16 v[122:125], v[138:141], v[162:165], v[122:125]
	v_mfma_f32_16x16x32_bf16 v[110:113], v[130:133], v[170:173], v[110:113]
	v_mfma_f32_16x16x32_bf16 v[106:109], v[138:141], v[170:173], v[106:109]
	v_mfma_f32_16x16x32_bf16 v[94:97], v[130:133], v[178:181], v[94:97]
	v_mfma_f32_16x16x32_bf16 v[90:93], v[138:141], v[178:181], v[90:93]
	v_mfma_f32_16x16x32_bf16 v[22:25], v[130:133], v[186:189], v[22:25]
	v_mfma_f32_16x16x32_bf16 v[10:13], v[138:141], v[186:189], v[10:13]
	v_mfma_f32_16x16x32_bf16 v[126:129], v[134:137], v[166:169], v[126:129]
	v_mfma_f32_16x16x32_bf16 v[122:125], v[142:145], v[166:169], v[122:125]
	v_mfma_f32_16x16x32_bf16 v[110:113], v[134:137], v[174:177], v[110:113]
	v_mfma_f32_16x16x32_bf16 v[106:109], v[142:145], v[174:177], v[106:109]
	v_mfma_f32_16x16x32_bf16 v[94:97], v[134:137], v[182:185], v[94:97]
	v_mfma_f32_16x16x32_bf16 v[90:93], v[142:145], v[182:185], v[90:93]
	v_mfma_f32_16x16x32_bf16 v[22:25], v[134:137], v[190:193], v[22:25]
	v_mfma_f32_16x16x32_bf16 v[10:13], v[142:145], v[190:193], v[10:13]
	v_mfma_f32_16x16x32_bf16 v[118:121], v[146:149], v[162:165], v[118:121]
	v_mfma_f32_16x16x32_bf16 v[114:117], v[154:157], v[162:165], v[114:117]
	v_mfma_f32_16x16x32_bf16 v[102:105], v[146:149], v[170:173], v[102:105]
	v_mfma_f32_16x16x32_bf16 v[98:101], v[154:157], v[170:173], v[98:101]
	v_mfma_f32_16x16x32_bf16 v[38:41], v[146:149], v[178:181], v[38:41]
	v_mfma_f32_16x16x32_bf16 v[26:29], v[154:157], v[178:181], v[26:29]
	v_mfma_f32_16x16x32_bf16 v[6:9], v[146:149], v[186:189], v[6:9]
	v_mfma_f32_16x16x32_bf16 v[2:5], v[154:157], v[186:189], v[2:5]
	v_mfma_f32_16x16x32_bf16 v[118:121], v[150:153], v[166:169], v[118:121]
	v_mfma_f32_16x16x32_bf16 v[114:117], v[158:161], v[166:169], v[114:117]
	v_mfma_f32_16x16x32_bf16 v[102:105], v[150:153], v[174:177], v[102:105]
	v_mfma_f32_16x16x32_bf16 v[98:101], v[158:161], v[174:177], v[98:101]
	v_mfma_f32_16x16x32_bf16 v[38:41], v[150:153], v[182:185], v[38:41]
	v_mfma_f32_16x16x32_bf16 v[26:29], v[158:161], v[182:185], v[26:29]
	v_mfma_f32_16x16x32_bf16 v[6:9], v[150:153], v[190:193], v[6:9]
	v_mfma_f32_16x16x32_bf16 v[2:5], v[158:161], v[190:193], v[2:5]
	s_barrier
	s_add_i32 s2, 0, 0x18000
	s_add_i32 s68, 0, 0x1c000
	v_add_u32_e32 v130, s2, v205
	v_add_u32_e32 v142, s68, v205
	ds_read_b128 v[146:149], v130
	ds_read_b128 v[150:153], v130 offset:1024
	ds_read_b128 v[154:157], v130 offset:2048
	ds_read_b128 v[158:161], v130 offset:3072
	ds_read_b128 v[130:133], v142
	ds_read_b128 v[134:137], v142 offset:1024
	ds_read_b128 v[138:141], v142 offset:2048
	ds_read_b128 v[142:145], v142 offset:3072
	s_add_u32 s64, s64, 0x20000
	s_addc_u32 s65, s65, 0
	s_mov_b32 m0, s52
	v_lshl_add_u64 v[218:219], s[64:65], 0, v[194:195]
	ds_read_b128 v[162:165], v209 offset:32768
	ds_read_b128 v[166:169], v209 offset:33792
	ds_read_b128 v[170:173], v209 offset:34816
	ds_read_b128 v[174:177], v209 offset:35840
	ds_read_b128 v[178:181], v209 offset:36864
	ds_read_b128 v[182:185], v209 offset:37888
	ds_read_b128 v[186:189], v209 offset:38912
	ds_read_b128 v[190:193], v209 offset:39936
	global_load_lds_dwordx4 v[218:219], off
	v_lshl_add_u64 v[218:219], s[64:65], 0, v[198:199]
	s_mov_b32 m0, s53
	s_nop 0
	global_load_lds_dwordx4 v[218:219], off
	s_waitcnt vmcnt(8)
	s_waitcnt lgkmcnt(0)
	s_barrier
	s_waitcnt lgkmcnt(0)
	v_mfma_f32_16x16x32_bf16 v[86:89], v[146:149], v[162:165], v[86:89]
	v_mfma_f32_16x16x32_bf16 v[82:85], v[154:157], v[162:165], v[82:85]
	v_mfma_f32_16x16x32_bf16 v[78:81], v[146:149], v[170:173], v[78:81]
	v_mfma_f32_16x16x32_bf16 v[74:77], v[154:157], v[170:173], v[74:77]
	v_mfma_f32_16x16x32_bf16 v[70:73], v[146:149], v[178:181], v[70:73]
	v_mfma_f32_16x16x32_bf16 v[66:69], v[154:157], v[178:181], v[66:69]
	v_mfma_f32_16x16x32_bf16 v[62:65], v[146:149], v[186:189], v[62:65]
	v_mfma_f32_16x16x32_bf16 v[58:61], v[154:157], v[186:189], v[58:61]
	v_mfma_f32_16x16x32_bf16 v[86:89], v[150:153], v[166:169], v[86:89]
	v_mfma_f32_16x16x32_bf16 v[82:85], v[158:161], v[166:169], v[82:85]
	v_mfma_f32_16x16x32_bf16 v[78:81], v[150:153], v[174:177], v[78:81]
	v_mfma_f32_16x16x32_bf16 v[74:77], v[158:161], v[174:177], v[74:77]
	v_mfma_f32_16x16x32_bf16 v[70:73], v[150:153], v[182:185], v[70:73]
	v_mfma_f32_16x16x32_bf16 v[66:69], v[158:161], v[182:185], v[66:69]
	v_mfma_f32_16x16x32_bf16 v[62:65], v[150:153], v[190:193], v[62:65]
	v_mfma_f32_16x16x32_bf16 v[58:61], v[158:161], v[190:193], v[58:61]
	v_mfma_f32_16x16x32_bf16 v[54:57], v[130:133], v[162:165], v[54:57]
	v_mfma_f32_16x16x32_bf16 v[50:53], v[138:141], v[162:165], v[50:53]
	v_mfma_f32_16x16x32_bf16 v[46:49], v[130:133], v[170:173], v[46:49]
	v_mfma_f32_16x16x32_bf16 v[42:45], v[138:141], v[170:173], v[42:45]
	v_mfma_f32_16x16x32_bf16 v[34:37], v[130:133], v[178:181], v[34:37]
	v_mfma_f32_16x16x32_bf16 v[30:33], v[138:141], v[178:181], v[30:33]
	v_mfma_f32_16x16x32_bf16 v[18:21], v[130:133], v[186:189], v[18:21]
	v_mfma_f32_16x16x32_bf16 v[14:17], v[138:141], v[186:189], v[14:17]
	v_mfma_f32_16x16x32_bf16 v[54:57], v[134:137], v[166:169], v[54:57]
	v_mfma_f32_16x16x32_bf16 v[50:53], v[142:145], v[166:169], v[50:53]
	v_mfma_f32_16x16x32_bf16 v[46:49], v[134:137], v[174:177], v[46:49]
	v_mfma_f32_16x16x32_bf16 v[42:45], v[142:145], v[174:177], v[42:45]
	v_mfma_f32_16x16x32_bf16 v[34:37], v[134:137], v[182:185], v[34:37]
	v_mfma_f32_16x16x32_bf16 v[30:33], v[142:145], v[182:185], v[30:33]
	v_mfma_f32_16x16x32_bf16 v[18:21], v[134:137], v[190:193], v[18:21]
	v_mfma_f32_16x16x32_bf16 v[14:17], v[142:145], v[190:193], v[14:17]
	s_barrier
	s_add_i32 s2, s2, s49
	v_lshl_add_u64 v[210:211], v[210:211], 0, s[12:13]
	s_mov_b32 m0, s2
	ds_read_b128 v[186:189], v209 offset:49152
	ds_read_b128 v[190:193], v209 offset:50176
	ds_read_b128 v[178:181], v209 offset:51200
	ds_read_b128 v[182:185], v209 offset:52224
	ds_read_b128 v[170:173], v209 offset:53248
	ds_read_b128 v[174:177], v209 offset:54272
	ds_read_b128 v[162:165], v209 offset:55296
	ds_read_b128 v[166:169], v209 offset:56320
	global_load_lds_dwordx4 v[210:211], off
	s_add_i32 m0, s2, 0x2000
	s_add_u32 s64, s66, 0x20080
	v_lshl_add_u64 v[210:211], v[212:213], 0, s[12:13]
	s_addc_u32 s65, s67, 0
	s_add_i32 s2, s68, s49
	global_load_lds_dwordx4 v[210:211], off
	v_lshl_add_u64 v[210:211], s[64:65], 0, v[196:197]
	s_mov_b32 m0, s2
	s_andn2_b64 vcc, exec, s[62:63]
	global_load_lds_dwordx4 v[210:211], off
	v_lshl_add_u64 v[210:211], s[64:65], 0, v[200:201]
	s_add_i32 m0, s2, 0x2000
	s_nop 0
	global_load_lds_dwordx4 v[210:211], off
	v_lshl_add_u64 v[210:211], v[214:215], 0, s[12:13]
	s_mov_b32 m0, s75
	s_nop 0
	global_load_lds_dwordx4 v[210:211], off
	v_lshl_add_u64 v[210:211], v[216:217], 0, s[12:13]
	s_mov_b32 m0, s76
	s_nop 0
	global_load_lds_dwordx4 v[210:211], off
	s_waitcnt vmcnt(8)
	s_waitcnt lgkmcnt(0)
	s_barrier
	s_cbranch_vccnz .LBB0_1936
	v_pk_mul_f32 v[214:215], v[86:87], s[20:21] op_sel_hi:[1,0]
	v_pk_mul_f32 v[216:217], v[82:83], s[20:21] op_sel_hi:[1,0]
	v_mov_b32_e32 v218, 0
	v_mov_b32_e32 v219, 0
	v_cvt_pk_fp8_f32 v218, v214, v215
	v_cvt_pk_fp8_f32 v219, v216, v217
	v_pk_mul_f32 v[214:215], v[88:89], s[20:21] op_sel_hi:[1,0]
	v_pk_mul_f32 v[216:217], v[84:85], s[20:21] op_sel_hi:[1,0]
	v_cvt_pk_fp8_f32 v218, v214, v215 op_sel:[0,0,1]
	v_cvt_pk_fp8_f32 v219, v216, v217 op_sel:[0,0,1]
	v_pk_mul_f32 v[214:215], v[54:55], s[20:21] op_sel_hi:[1,0]
	v_pk_mul_f32 v[216:217], v[50:51], s[20:21] op_sel_hi:[1,0]
	v_mov_b32_e32 v220, 0
	v_mov_b32_e32 v221, 0
	v_mov_b32_e32 v210, v1
	v_mov_b32_e32 v211, v204
	v_cvt_pk_fp8_f32 v220, v214, v215
	v_cvt_pk_fp8_f32 v221, v216, v217
	v_pk_mul_f32 v[214:215], v[56:57], s[20:21] op_sel_hi:[1,0]
	v_add_u32_e32 v210, s87, v210
	v_lshl_add_u32 v212, v211, 3, s88
	v_ashrrev_i32_e32 v211, 31, v210
	v_pk_mul_f32 v[216:217], v[52:53], s[20:21] op_sel_hi:[1,0]
	v_lshlrev_b64 v[210:211], 11, v[210:211]
	v_cvt_pk_fp8_f32 v220, v214, v215 op_sel:[0,0,1]
	v_cvt_pk_fp8_f32 v221, v216, v217 op_sel:[0,0,1]
	v_ashrrev_i32_e32 v213, 31, v212
	v_lshl_add_u64 v[210:211], s[10:11], 0, v[210:211]
	v_lshl_add_u64 v[210:211], v[210:211], 0, v[212:213]
	s_nop 1
	v_permlane16_swap_b32 v218, v220
	v_permlane16_swap_b32 v219, v221
	v_and_b32_e32 v216, 1, v204
	v_mul_u32_u24_e32 v216, 0x78, v216
	v_mov_b32_e32 v217, 0
	v_lshl_add_u64 v[216:217], v[210:211], 0, v[216:217]
	global_store_dwordx4 v[216:217], v[218:221], off
	v_pk_mul_f32 v[214:215], v[78:79], s[20:21] op_sel_hi:[1,0]
	v_pk_mul_f32 v[216:217], v[74:75], s[20:21] op_sel_hi:[1,0]
	v_mov_b32_e32 v218, 0
	v_mov_b32_e32 v219, 0
	v_cvt_pk_fp8_f32 v218, v214, v215
	v_cvt_pk_fp8_f32 v219, v216, v217
	v_pk_mul_f32 v[214:215], v[80:81], s[20:21] op_sel_hi:[1,0]
	v_pk_mul_f32 v[216:217], v[76:77], s[20:21] op_sel_hi:[1,0]
	v_cvt_pk_fp8_f32 v218, v214, v215 op_sel:[0,0,1]
	v_cvt_pk_fp8_f32 v219, v216, v217 op_sel:[0,0,1]
	v_pk_mul_f32 v[214:215], v[46:47], s[20:21] op_sel_hi:[1,0]
	v_pk_mul_f32 v[216:217], v[42:43], s[20:21] op_sel_hi:[1,0]
	v_mov_b32_e32 v220, 0
	v_mov_b32_e32 v221, 0
	v_cvt_pk_fp8_f32 v220, v214, v215
	v_cvt_pk_fp8_f32 v221, v216, v217
	v_pk_mul_f32 v[214:215], v[48:49], s[20:21] op_sel_hi:[1,0]
	v_pk_mul_f32 v[216:217], v[44:45], s[20:21] op_sel_hi:[1,0]
	v_cvt_pk_fp8_f32 v220, v214, v215 op_sel:[0,0,1]
	v_cvt_pk_fp8_f32 v221, v216, v217 op_sel:[0,0,1]
	s_mov_b32 s2, 0x8000
	v_add_co_u32_e32 v214, vcc, s2, v210
	v_lshl_add_u64 v[212:213], v[210:211], 0, s[24:25]
	s_nop 0
	v_addc_co_u32_e32 v215, vcc, 0, v211, vcc
	s_nop 1
	v_permlane16_swap_b32 v218, v220
	v_permlane16_swap_b32 v219, v221
	v_and_b32_e32 v216, 1, v204
	v_mul_u32_u24_e32 v216, 0x78, v216
	v_mov_b32_e32 v217, 0
	v_lshl_add_u64 v[216:217], v[214:215], 0, v[216:217]
	global_store_dwordx4 v[216:217], v[218:221], off
	v_pk_mul_f32 v[214:215], v[70:71], s[20:21] op_sel_hi:[1,0]
	v_pk_mul_f32 v[216:217], v[66:67], s[20:21] op_sel_hi:[1,0]
	v_mov_b32_e32 v218, 0
	v_mov_b32_e32 v219, 0
	v_cvt_pk_fp8_f32 v218, v214, v215
	v_cvt_pk_fp8_f32 v219, v216, v217
	v_pk_mul_f32 v[214:215], v[72:73], s[20:21] op_sel_hi:[1,0]
	v_pk_mul_f32 v[216:217], v[68:69], s[20:21] op_sel_hi:[1,0]
	v_cvt_pk_fp8_f32 v218, v214, v215 op_sel:[0,0,1]
	v_cvt_pk_fp8_f32 v219, v216, v217 op_sel:[0,0,1]
	v_pk_mul_f32 v[214:215], v[34:35], s[20:21] op_sel_hi:[1,0]
	v_pk_mul_f32 v[216:217], v[30:31], s[20:21] op_sel_hi:[1,0]
	v_mov_b32_e32 v220, 0
	v_mov_b32_e32 v221, 0
	v_cvt_pk_fp8_f32 v220, v214, v215
	v_cvt_pk_fp8_f32 v221, v216, v217
	v_pk_mul_f32 v[214:215], v[36:37], s[20:21] op_sel_hi:[1,0]
	v_pk_mul_f32 v[216:217], v[32:33], s[20:21] op_sel_hi:[1,0]
	v_cvt_pk_fp8_f32 v220, v214, v215 op_sel:[0,0,1]
	v_cvt_pk_fp8_f32 v221, v216, v217 op_sel:[0,0,1]
	s_mov_b32 s2, 0x10000
	v_add_co_u32_e32 v214, vcc, s2, v210
	v_lshl_add_u64 v[212:213], v[210:211], 0, s[28:29]
	s_nop 0
	v_addc_co_u32_e32 v215, vcc, 0, v211, vcc
	s_nop 1
	v_permlane16_swap_b32 v218, v220
	v_permlane16_swap_b32 v219, v221
	v_and_b32_e32 v216, 1, v204
	v_mul_u32_u24_e32 v216, 0x78, v216
	v_mov_b32_e32 v217, 0
	v_lshl_add_u64 v[216:217], v[214:215], 0, v[216:217]
	global_store_dwordx4 v[216:217], v[218:221], off
	v_pk_mul_f32 v[214:215], v[62:63], s[20:21] op_sel_hi:[1,0]
	v_pk_mul_f32 v[216:217], v[58:59], s[20:21] op_sel_hi:[1,0]
	v_mov_b32_e32 v218, 0
	v_mov_b32_e32 v219, 0
	v_cvt_pk_fp8_f32 v218, v214, v215
	v_cvt_pk_fp8_f32 v219, v216, v217
	v_pk_mul_f32 v[214:215], v[64:65], s[20:21] op_sel_hi:[1,0]
	v_pk_mul_f32 v[216:217], v[60:61], s[20:21] op_sel_hi:[1,0]
	v_cvt_pk_fp8_f32 v218, v214, v215 op_sel:[0,0,1]
	v_cvt_pk_fp8_f32 v219, v216, v217 op_sel:[0,0,1]
	v_pk_mul_f32 v[214:215], v[18:19], s[20:21] op_sel_hi:[1,0]
	v_pk_mul_f32 v[216:217], v[14:15], s[20:21] op_sel_hi:[1,0]
	v_mov_b32_e32 v220, 0
	v_mov_b32_e32 v221, 0
	v_cvt_pk_fp8_f32 v220, v214, v215
	v_cvt_pk_fp8_f32 v221, v216, v217
	v_pk_mul_f32 v[214:215], v[20:21], s[20:21] op_sel_hi:[1,0]
	v_pk_mul_f32 v[216:217], v[16:17], s[20:21] op_sel_hi:[1,0]
	v_cvt_pk_fp8_f32 v220, v214, v215 op_sel:[0,0,1]
	v_cvt_pk_fp8_f32 v221, v216, v217 op_sel:[0,0,1]
	s_mov_b32 s2, 0x18000
	v_lshl_add_u64 v[212:213], v[210:211], 0, s[30:31]
	v_add_co_u32_e32 v210, vcc, s2, v210
	s_nop 1
	v_addc_co_u32_e32 v211, vcc, 0, v211, vcc
	s_nop 1
	v_permlane16_swap_b32 v218, v220
	v_permlane16_swap_b32 v219, v221
	v_and_b32_e32 v216, 1, v204
	v_mul_u32_u24_e32 v216, 0x78, v216
	v_mov_b32_e32 v217, 0
	v_lshl_add_u64 v[216:217], v[210:211], 0, v[216:217]
	global_store_dwordx4 v[216:217], v[218:221], off
	s_branch .LBB0_1936

.LBB0_1958:
	v_pk_mul_f32 v[20:21], v[126:127], s[20:21] op_sel_hi:[1,0]
	v_pk_mul_f32 v[30:31], v[122:123], s[20:21] op_sel_hi:[1,0]
	v_mov_b32_e32 v32, 0
	v_mov_b32_e32 v33, 0
	v_cvt_pk_fp8_f32 v32, v20, v21
	v_cvt_pk_fp8_f32 v33, v30, v31
	v_pk_mul_f32 v[20:21], v[128:129], s[20:21] op_sel_hi:[1,0]
	v_pk_mul_f32 v[30:31], v[124:125], s[20:21] op_sel_hi:[1,0]
	v_cvt_pk_fp8_f32 v32, v20, v21 op_sel:[0,0,1]
	v_cvt_pk_fp8_f32 v33, v30, v31 op_sel:[0,0,1]
	v_pk_mul_f32 v[20:21], v[118:119], s[20:21] op_sel_hi:[1,0]
	v_pk_mul_f32 v[30:31], v[114:115], s[20:21] op_sel_hi:[1,0]
	v_mov_b32_e32 v34, 0
	v_mov_b32_e32 v35, 0
	v_cvt_pk_fp8_f32 v34, v20, v21
	v_cvt_pk_fp8_f32 v35, v30, v31
	v_add_u32_e32 v16, s35, v206
	v_ashrrev_i32_e32 v17, 31, v16
	v_pk_mul_f32 v[20:21], v[120:121], s[20:21] op_sel_hi:[1,0]
	v_pk_mul_f32 v[30:31], v[116:117], s[20:21] op_sel_hi:[1,0]
	v_or_b32_e32 v14, s86, v207
	v_lshlrev_b64 v[18:19], 11, v[16:17]
	v_cvt_pk_fp8_f32 v34, v20, v21 op_sel:[0,0,1]
	v_cvt_pk_fp8_f32 v35, v30, v31 op_sel:[0,0,1]
	v_ashrrev_i32_e32 v15, 31, v14
	v_lshl_add_u64 v[18:19], s[10:11], 0, v[18:19]
	v_lshl_add_u64 v[18:19], v[18:19], 0, v[14:15]
	s_nop 1
	v_permlane16_swap_b32 v32, v34
	v_permlane16_swap_b32 v33, v35
	v_and_b32_e32 v30, 1, v204
	v_mul_u32_u24_e32 v30, 0x78, v30
	v_mov_b32_e32 v31, 0
	v_lshl_add_u64 v[30:31], v[18:19], 0, v[30:31]
	global_store_dwordx4 v[30:31], v[32:35], off
	v_pk_mul_f32 v[20:21], v[110:111], s[20:21] op_sel_hi:[1,0]
	v_pk_mul_f32 v[30:31], v[106:107], s[20:21] op_sel_hi:[1,0]
	v_mov_b32_e32 v32, 0
	v_mov_b32_e32 v33, 0
	v_cvt_pk_fp8_f32 v32, v20, v21
	v_cvt_pk_fp8_f32 v33, v30, v31
	v_pk_mul_f32 v[20:21], v[112:113], s[20:21] op_sel_hi:[1,0]
	v_pk_mul_f32 v[30:31], v[108:109], s[20:21] op_sel_hi:[1,0]
	v_cvt_pk_fp8_f32 v32, v20, v21 op_sel:[0,0,1]
	v_cvt_pk_fp8_f32 v33, v30, v31 op_sel:[0,0,1]
	v_pk_mul_f32 v[20:21], v[102:103], s[20:21] op_sel_hi:[1,0]
	v_pk_mul_f32 v[30:31], v[98:99], s[20:21] op_sel_hi:[1,0]
	v_mov_b32_e32 v34, 0
	v_mov_b32_e32 v35, 0
	v_cvt_pk_fp8_f32 v34, v20, v21
	v_cvt_pk_fp8_f32 v35, v30, v31
	v_or_b32_e32 v18, 16, v16
	v_ashrrev_i32_e32 v19, 31, v18
	v_pk_mul_f32 v[20:21], v[104:105], s[20:21] op_sel_hi:[1,0]
	v_pk_mul_f32 v[30:31], v[100:101], s[20:21] op_sel_hi:[1,0]
	v_lshlrev_b64 v[18:19], 11, v[18:19]
	v_cvt_pk_fp8_f32 v34, v20, v21 op_sel:[0,0,1]
	v_cvt_pk_fp8_f32 v35, v30, v31 op_sel:[0,0,1]
	v_lshl_add_u64 v[18:19], s[10:11], 0, v[18:19]
	v_lshl_add_u64 v[18:19], v[18:19], 0, v[14:15]
	s_nop 1
	v_permlane16_swap_b32 v32, v34
	v_permlane16_swap_b32 v33, v35
	v_and_b32_e32 v30, 1, v204
	v_mul_u32_u24_e32 v30, 0x78, v30
	v_mov_b32_e32 v31, 0
	v_lshl_add_u64 v[30:31], v[18:19], 0, v[30:31]
	global_store_dwordx4 v[30:31], v[32:35], off
	v_pk_mul_f32 v[20:21], v[94:95], s[20:21] op_sel_hi:[1,0]
	v_pk_mul_f32 v[30:31], v[90:91], s[20:21] op_sel_hi:[1,0]
	v_mov_b32_e32 v46, 0
	v_mov_b32_e32 v47, 0
	v_cvt_pk_fp8_f32 v46, v20, v21
	v_cvt_pk_fp8_f32 v47, v30, v31
	v_pk_mul_f32 v[20:21], v[96:97], s[20:21] op_sel_hi:[1,0]
	v_pk_mul_f32 v[30:31], v[92:93], s[20:21] op_sel_hi:[1,0]
	v_cvt_pk_fp8_f32 v46, v20, v21 op_sel:[0,0,1]
	v_cvt_pk_fp8_f32 v47, v30, v31 op_sel:[0,0,1]
	v_pk_mul_f32 v[20:21], v[38:39], s[20:21] op_sel_hi:[1,0]
	v_pk_mul_f32 v[26:27], v[26:27], s[20:21] op_sel_hi:[1,0]
	v_mov_b32_e32 v48, 0
	v_mov_b32_e32 v49, 0
	v_cvt_pk_fp8_f32 v48, v20, v21
	v_cvt_pk_fp8_f32 v49, v26, v27
	v_or_b32_e32 v18, 32, v16
	v_ashrrev_i32_e32 v19, 31, v18
	v_pk_mul_f32 v[20:21], v[40:41], s[20:21] op_sel_hi:[1,0]
	v_pk_mul_f32 v[26:27], v[28:29], s[20:21] op_sel_hi:[1,0]
	v_lshlrev_b64 v[18:19], 11, v[18:19]
	v_cvt_pk_fp8_f32 v48, v20, v21 op_sel:[0,0,1]
	v_cvt_pk_fp8_f32 v49, v26, v27 op_sel:[0,0,1]
	v_lshl_add_u64 v[18:19], s[10:11], 0, v[18:19]
	v_lshl_add_u64 v[18:19], v[18:19], 0, v[14:15]
	s_nop 1
	v_permlane16_swap_b32 v46, v48
	v_permlane16_swap_b32 v47, v49
	v_and_b32_e32 v26, 1, v204
	v_mul_u32_u24_e32 v26, 0x78, v26
	v_mov_b32_e32 v27, 0
	v_lshl_add_u64 v[26:27], v[18:19], 0, v[26:27]
	global_store_dwordx4 v[26:27], v[46:49], off
	v_pk_mul_f32 v[18:19], v[22:23], s[20:21] op_sel_hi:[1,0]
	v_mov_b32_e32 v20, 0
	v_cvt_pk_fp8_f32 v20, v18, v19
	v_pk_mul_f32 v[10:11], v[10:11], s[20:21] op_sel_hi:[1,0]
	v_mov_b32_e32 v21, 0
	v_cvt_pk_fp8_f32 v21, v10, v11
	v_pk_mul_f32 v[10:11], v[24:25], s[20:21] op_sel_hi:[1,0]
	v_pk_mul_f32 v[6:7], v[6:7], s[20:21] op_sel_hi:[1,0]
	v_cvt_pk_fp8_f32 v20, v10, v11 op_sel:[0,0,1]
	v_pk_mul_f32 v[2:3], v[2:3], s[20:21] op_sel_hi:[1,0]
	v_mov_b32_e32 v10, 0
	v_mov_b32_e32 v11, 0
	v_cvt_pk_fp8_f32 v10, v6, v7
	v_cvt_pk_fp8_f32 v11, v2, v3
	v_or_b32_e32 v16, 48, v16
	v_pk_mul_f32 v[12:13], v[12:13], s[20:21] op_sel_hi:[1,0]
	v_ashrrev_i32_e32 v17, 31, v16
	v_cvt_pk_fp8_f32 v21, v12, v13 op_sel:[0,0,1]
	v_pk_mul_f32 v[2:3], v[8:9], s[20:21] op_sel_hi:[1,0]
	v_pk_mul_f32 v[4:5], v[4:5], s[20:21] op_sel_hi:[1,0]
	v_lshlrev_b64 v[16:17], 11, v[16:17]
	v_cvt_pk_fp8_f32 v10, v2, v3 op_sel:[0,0,1]
	v_cvt_pk_fp8_f32 v11, v4, v5 op_sel:[0,0,1]
	v_lshl_add_u64 v[2:3], s[10:11], 0, v[16:17]
	v_lshl_add_u64 v[2:3], v[2:3], 0, v[14:15]
	s_andn2_b64 vcc, exec, s[54:55]
	s_mov_b64 s[38:39], -1
	global_store_dwordx2 v[2:3], v[20:21], off
	global_store_dwordx2 v[2:3], v[10:11], off offset:128
	s_cbranch_vccnz .LBB0_1925
	s_andn2_b64 vcc, exec, s[8:9]
	s_cbranch_vccnz .LBB0_1924
	s_barrier
	s_branch .LBB0_1924
